# k_iter first: candidate table built three 512-source rounds per pass (one count exchange and barrier pair instead of three)
# speedup vs baseline: 1.0158x; 1.0158x over previous
.LBB2_10:
	s_or_b64 exec, exec, s[10:11]
	s_waitcnt lgkmcnt(1)
	v_add_u32_e32 v1, v15, v14
	v_add_u32_e32 v1, v1, v16
	v_add_u32_e32 v1, v1, v17
	s_waitcnt lgkmcnt(0)
	v_add_u32_e32 v1, v1, v10
	v_add_u32_e32 v1, v1, v11
	s_load_dwordx2 s[48:49], s[0:1], 0x90
	s_load_dwordx2 s[50:51], s[0:1], 0x80
	s_load_dwordx4 s[28:31], s[0:1], 0x60
	s_load_dwordx2 s[34:35], s[0:1], 0x48
	v_add_u32_e32 v1, v1, v12
	v_add_u32_e32 v1, v1, v13
	s_lshr_b32 s27, s54, 6
	v_readfirstlane_b32 s2, v1
	s_lshl_b32 s60, s2, 3
	s_lshl_b64 s[20:21], s[46:47], 16
	s_add_u32 s44, s6, s20
	s_addc_u32 s45, s7, s21
	s_cmp_lt_i32 s2, 1
	s_waitcnt lgkmcnt(0)
	s_barrier
	s_cbranch_scc1 .LBB2_20
	s_lshl_b32 s47, s27, 2
	s_addk_i32 s47, 0x6000
	s_cmpk_gt_u32 s54, 0x1ff
	s_cselect_b64 s[2:3], -1, 0
	s_cmpk_gt_u32 s54, 0x1bf
	s_cselect_b64 s[4:5], -1, 0
	s_cmpk_gt_u32 s54, 0x17f
	s_cselect_b64 s[6:7], -1, 0
	s_cmpk_gt_u32 s54, 0x13f
	s_cselect_b64 s[10:11], -1, 0
	s_cmpk_gt_u32 s54, 0xff
	s_load_dwordx2 s[22:23], s[0:1], 0x88
	s_load_dwordx4 s[40:43], s[0:1], 0x0
	s_load_dwordx2 s[52:53], s[0:1], 0x10
	s_cselect_b64 s[12:13], -1, 0
	s_cmpk_gt_u32 s54, 0xbf
	s_cselect_b64 s[14:15], -1, 0
	s_cmpk_gt_u32 s54, 0x7f
	s_cselect_b64 s[16:17], -1, 0
	s_cmp_lt_u32 s54, 64
	s_cselect_b64 s[54:55], -1, 0
	s_waitcnt lgkmcnt(0)
	s_add_u32 s20, s22, s20
	v_mov_b32_e32 v7, 0
	s_addc_u32 s21, s23, s21
	v_lshl_add_u64 v[10:11], s[20:21], 0, v[6:7]
	v_and_b32_e32 v5, 7, v0
	v_not_b32_e32 v1, v19
	v_not_b32_e32 v24, v18
	v_lshl_add_u64 v[26:27], v[10:11], 0, 8
	v_lshrrev_b32_e32 v9, 3, v0
	s_mov_b32 s61, 0
	s_mov_b32 s62, 0x3d23dc48
	s_movk_i32 s63, 0x600
	s_mov_b64 s[56:57], 0x2000
	v_mov_b32_e32 v30, 0xff800000
	v_mov_b32_e32 v6, 0
	s_mov_b32 s91, 0
.Lb3_top:
	v_add_u32_e32 v216, s61, v0
	v_add_u32_e32 v217, 0x200, v216
	v_add_u32_e32 v218, 0x400, v216
	v_cmp_gt_i32_e64 s[66:67], s60, v216
	v_cmp_gt_i32_e64 s[68:69], s60, v217
	v_cmp_gt_i32_e64 s[70:71], s60, v218
	v_add_u32_e32 v220, 64, v9
	v_add_u32_e32 v221, 0x80, v9
	v_cndmask_b32_e64 v219, 0, v9, s[66:67]
	v_cndmask_b32_e64 v220, 0, v220, s[68:69]
	v_cndmask_b32_e64 v221, 0, v221, s[70:71]
	v_lshlrev_b32_e32 v219, 2, v219
	v_lshlrev_b32_e32 v220, 2, v220
	v_lshlrev_b32_e32 v221, 2, v221
	ds_read_b32 v219, v219 offset:24576
	ds_read_b32 v220, v220 offset:24576
	ds_read_b32 v221, v221 offset:24576
	s_waitcnt lgkmcnt(0)
	v_lshl_or_b32 v219, v219, 3, v5
	v_lshl_or_b32 v220, v220, 3, v5
	v_lshl_or_b32 v221, v221, 3, v5
	v_add_lshl_u32 v222, v219, s58, 2
	v_add_lshl_u32 v223, v220, s58, 2
	v_add_lshl_u32 v224, v221, s58, 2
	global_load_dword v226, v222, s[40:41]
	global_load_dword v227, v222, s[42:43]
	global_load_dword v228, v222, s[52:53]
	global_load_dword v230, v223, s[40:41]
	global_load_dword v231, v223, s[42:43]
	global_load_dword v232, v223, s[52:53]
	global_load_dword v234, v224, s[40:41]
	global_load_dword v235, v224, s[42:43]
	global_load_dword v236, v224, s[52:53]
	v_lshlrev_b32_e32 v216, 4, v216
	v_lshlrev_b32_e32 v217, 4, v217
	v_lshlrev_b32_e32 v218, 4, v218
	s_waitcnt vmcnt(0)
	v_pk_add_f32 v[238:239], v[226:227], v[22:23] neg_lo:[0,1] neg_hi:[0,1]
	v_mov_b32_e32 v241, v219
	v_pk_mul_f32 v[250:251], v[238:239], v[238:239]
	v_cmp_ne_u32_e64 s[72:73], 0, v228
	v_sub_f32_e32 v252, s36, v226
	v_add_f32_e32 v240, v250, v251
	v_mul_f32_e32 v240, 0xc31044f5, v240
	v_cndmask_b32_e64 v240, v30, v240, s[72:73]
	s_mov_b64 exec, s[66:67]
	global_store_dwordx4 v216, v[238:241], s[20:21] sc1
	s_mov_b64 exec, -1
	v_subrev_f32_e32 v253, s38, v226
	v_max3_f32 v252, v252, v253, 0
	v_sub_f32_e32 v253, s37, v227
	v_subrev_f32_e32 v254, s39, v227
	v_max3_f32 v253, v253, v254, 0
	v_pk_mul_f32 v[252:253], v[252:253], v[252:253]
	s_nop 0
	v_add_f32_e32 v252, v252, v253
	v_cmp_gt_f32_e64 s[74:75], s62, v252
	s_and_b64 s[72:73], s[72:73], s[74:75]
	s_and_b64 s[76:77], s[66:67], s[72:73]
	s_bcnt1_i32_b64 s82, s[76:77]
	v_pk_add_f32 v[242:243], v[230:231], v[22:23] neg_lo:[0,1] neg_hi:[0,1]
	v_mov_b32_e32 v245, v220
	v_pk_mul_f32 v[250:251], v[242:243], v[242:243]
	v_cmp_ne_u32_e64 s[72:73], 0, v232
	v_sub_f32_e32 v252, s36, v230
	v_add_f32_e32 v244, v250, v251
	v_mul_f32_e32 v244, 0xc31044f5, v244
	v_cndmask_b32_e64 v244, v30, v244, s[72:73]
	s_mov_b64 exec, s[68:69]
	global_store_dwordx4 v217, v[242:245], s[20:21] sc1
	s_mov_b64 exec, -1
	v_subrev_f32_e32 v253, s38, v230
	v_max3_f32 v252, v252, v253, 0
	v_sub_f32_e32 v253, s37, v231
	v_subrev_f32_e32 v254, s39, v231
	v_max3_f32 v253, v253, v254, 0
	v_pk_mul_f32 v[252:253], v[252:253], v[252:253]
	s_nop 0
	v_add_f32_e32 v252, v252, v253
	v_cmp_gt_f32_e64 s[74:75], s62, v252
	s_and_b64 s[72:73], s[72:73], s[74:75]
	s_and_b64 s[78:79], s[68:69], s[72:73]
	s_bcnt1_i32_b64 s83, s[78:79]
	v_pk_add_f32 v[246:247], v[234:235], v[22:23] neg_lo:[0,1] neg_hi:[0,1]
	v_mov_b32_e32 v249, v221
	v_pk_mul_f32 v[250:251], v[246:247], v[246:247]
	v_cmp_ne_u32_e64 s[72:73], 0, v236
	v_sub_f32_e32 v252, s36, v234
	v_add_f32_e32 v248, v250, v251
	v_mul_f32_e32 v248, 0xc31044f5, v248
	v_cndmask_b32_e64 v248, v30, v248, s[72:73]
	s_mov_b64 exec, s[70:71]
	global_store_dwordx4 v218, v[246:249], s[20:21] sc1
	s_mov_b64 exec, -1
	v_subrev_f32_e32 v253, s38, v234
	v_max3_f32 v252, v252, v253, 0
	v_sub_f32_e32 v253, s37, v235
	v_subrev_f32_e32 v254, s39, v235
	v_max3_f32 v253, v253, v254, 0
	v_pk_mul_f32 v[252:253], v[252:253], v[252:253]
	s_nop 0
	v_add_f32_e32 v252, v252, v253
	v_cmp_gt_f32_e64 s[74:75], s62, v252
	s_and_b64 s[72:73], s[72:73], s[74:75]
	s_and_b64 s[80:81], s[70:71], s[72:73]
	s_bcnt1_i32_b64 s84, s[80:81]
	v_mov_b32_e32 v250, s82
	v_mov_b32_e32 v251, s83
	v_mov_b32_e32 v252, s84
	v_mov_b32_e32 v253, s47
	s_and_saveexec_b64 s[22:23], vcc
	ds_write_b32 v253, v250 offset:3104
	ds_write_b32 v253, v251 offset:3136
	ds_write_b32 v253, v252 offset:3168
	s_or_b64 exec, exec, s[22:23]
	s_waitcnt lgkmcnt(0)
	s_barrier
	v_lshlrev_b32_e32 v250, 2, v44
	ds_read_b32 v250, v250 offset:27680
	v_cmp_gt_u32_e64 s[72:73], 24, v44
	s_add_i32 s85, s27, 8
	s_add_i32 s86, s27, 16
	s_waitcnt lgkmcnt(0)
	v_cndmask_b32_e64 v250, 0, v250, s[72:73]
	s_nop 1
	v_add_u32_dpp v251, v250, v250 row_shr:1 row_mask:0xf bank_mask:0xf bound_ctrl:1
	s_nop 1
	v_add_u32_dpp v251, v251, v251 row_shr:2 row_mask:0xf bank_mask:0xf bound_ctrl:1
	s_nop 1
	v_add_u32_dpp v251, v251, v251 row_shr:4 row_mask:0xf bank_mask:0xf bound_ctrl:1
	s_nop 1
	v_add_u32_dpp v251, v251, v251 row_shr:8 row_mask:0xf bank_mask:0xf bound_ctrl:1
	s_nop 1
	v_add_u32_dpp v251, v251, v251 row_bcast:15 row_mask:0xa bank_mask:0xf
	v_sub_u32_e32 v252, v251, v250
	s_nop 1
	v_readlane_b32 s87, v252, s27
	v_readlane_b32 s88, v252, s85
	v_readlane_b32 s89, v252, s86
	v_readlane_b32 s90, v251, 23
	s_nop 1
	s_add_i32 s87, s87, s91
	v_mbcnt_lo_u32_b32 v253, s76, 0
	v_mbcnt_hi_u32_b32 v253, s77, v253
	v_add_u32_e32 v253, s87, v253
	v_lshlrev_b32_e32 v254, 4, v253
	v_cmp_gt_u32_e64 s[72:73], s63, v253
	s_mov_b64 exec, s[76:77]
	global_store_dwordx4 v254, v[238:241], s[44:45] sc1
	s_and_b64 exec, exec, s[72:73]
	ds_write_b128 v254, v[238:241]
	s_mov_b64 exec, -1
	s_add_i32 s88, s88, s91
	v_mbcnt_lo_u32_b32 v253, s78, 0
	v_mbcnt_hi_u32_b32 v253, s79, v253
	v_add_u32_e32 v253, s88, v253
	v_lshlrev_b32_e32 v254, 4, v253
	v_cmp_gt_u32_e64 s[72:73], s63, v253
	s_mov_b64 exec, s[78:79]
	global_store_dwordx4 v254, v[242:245], s[44:45] sc1
	s_and_b64 exec, exec, s[72:73]
	ds_write_b128 v254, v[242:245]
	s_mov_b64 exec, -1
	s_add_i32 s89, s89, s91
	v_mbcnt_lo_u32_b32 v253, s80, 0
	v_mbcnt_hi_u32_b32 v253, s81, v253
	v_add_u32_e32 v253, s89, v253
	v_lshlrev_b32_e32 v254, 4, v253
	v_cmp_gt_u32_e64 s[72:73], s63, v253
	s_mov_b64 exec, s[80:81]
	global_store_dwordx4 v254, v[246:249], s[44:45] sc1
	s_and_b64 exec, exec, s[72:73]
	ds_write_b128 v254, v[246:249]
	s_mov_b64 exec, -1
	s_add_i32 s91, s91, s90
	s_addk_i32 s61, 0x600
	v_add_u32_e32 v9, 0xc0, v9
	s_cmp_ge_i32 s61, s60
	s_waitcnt lgkmcnt(0)
	s_barrier
	s_cbranch_scc0 .Lb3_top
	v_mov_b32_e32 v6, s91
	s_branch .LBB2_21

	.amdhsa_kernel _Z6k_iterILb1ELb0EEvPKfS1_PKiPK15HIP_vector_typeIfLj4EES7_S1_S1_S3_S1_PfS8_S1_S3_PDF16_PS5_SA_PiSA_SB_
		.amdhsa_group_segment_fixed_size 30384
		.amdhsa_private_segment_fixed_size 0
		.amdhsa_kernarg_size 152
		.amdhsa_user_sgpr_count 2
		.amdhsa_user_sgpr_dispatch_ptr 0
		.amdhsa_user_sgpr_queue_ptr 0
		.amdhsa_user_sgpr_kernarg_segment_ptr 1
		.amdhsa_user_sgpr_dispatch_id 0
		.amdhsa_user_sgpr_kernarg_preload_length 0
		.amdhsa_user_sgpr_kernarg_preload_offset 0
		.amdhsa_user_sgpr_private_segment_size 0
		.amdhsa_uses_dynamic_stack 0
		.amdhsa_enable_private_segment 0
		.amdhsa_system_sgpr_workgroup_id_x 1
		.amdhsa_system_sgpr_workgroup_id_y 0
		.amdhsa_system_sgpr_workgroup_id_z 0
		.amdhsa_system_sgpr_workgroup_info 0
		.amdhsa_system_vgpr_workitem_id 0
		.amdhsa_next_free_vgpr 256
		.amdhsa_next_free_sgpr 96
		.amdhsa_accum_offset 256
		.amdhsa_reserve_vcc 1
		.amdhsa_float_round_mode_32 0
		.amdhsa_float_round_mode_16_64 0
		.amdhsa_float_denorm_mode_32 3
		.amdhsa_float_denorm_mode_16_64 3
		.amdhsa_dx10_clamp 1
		.amdhsa_ieee_mode 1
		.amdhsa_fp16_overflow 0
		.amdhsa_tg_split 0
		.amdhsa_exception_fp_ieee_invalid_op 0
		.amdhsa_exception_fp_denorm_src 0
		.amdhsa_exception_fp_ieee_div_zero 0
		.amdhsa_exception_fp_ieee_overflow 0
		.amdhsa_exception_fp_ieee_underflow 0
		.amdhsa_exception_fp_ieee_inexact 0
		.amdhsa_exception_int_div_zero 0
	.end_amdhsa_kernel

.LBB4_39:
	s_waitcnt vmcnt(5)
	v_rcp_f32_e32 v2, v133
	s_waitcnt vmcnt(4)
	v_rcp_f32_e32 v3, v132
	s_waitcnt vmcnt(3)
	v_rcp_f32_e32 v4, v131
	v_cmp_lt_f32_e32 vcc, 0, v133
	s_waitcnt vmcnt(2)
	v_rcp_f32_e32 v5, v130
	s_waitcnt vmcnt(1)
	v_rcp_f32_e32 v6, v129
	v_cndmask_b32_e32 v2, 0, v2, vcc
	v_cmp_lt_f32_e32 vcc, 0, v132
	s_waitcnt vmcnt(0)
	v_rcp_f32_e32 v7, v128
	s_getpc_b64 s[36:37]
	s_sub_u32 s36, s36, 0x922c
	s_subb_u32 s37, s37, 0
	v_lshlrev_b32_e32 v183, 6, v0
	v_min_u32_e32 v183, 0x1980, v183
	global_load_dword v183, v183, s[36:37]
	s_mov_b32 s4, 0x42c80000
	v_cndmask_b32_e32 v3, 0, v3, vcc
	v_cmp_lt_f32_e32 vcc, 0, v131
	v_cmp_ngt_f32_e64 s[2:3], s4, v3
	s_mov_b64 s[6:7], 0
	v_cndmask_b32_e32 v4, 0, v4, vcc
	v_cmp_lt_f32_e32 vcc, 0, v130
	s_nop 1
	v_cndmask_b32_e32 v5, 0, v5, vcc
	v_cmp_lt_f32_e32 vcc, 0, v129
	s_nop 1
	v_cndmask_b32_e32 v6, 0, v6, vcc
	v_cmp_lt_f32_e32 vcc, 0, v128
	s_nop 1
	v_cndmask_b32_e32 v7, 0, v7, vcc
	v_cmp_ngt_f32_e32 vcc, s4, v2
	s_or_b64 s[2:3], vcc, s[2:3]
	v_cmp_ngt_f32_e32 vcc, s4, v4
	s_or_b64 s[2:3], s[2:3], vcc
	v_cmp_ngt_f32_e32 vcc, s4, v5
	s_or_b64 s[2:3], s[2:3], vcc
	v_cmp_ngt_f32_e32 vcc, s4, v6
	s_or_b64 s[2:3], s[2:3], vcc
	v_cmp_ngt_f32_e32 vcc, s4, v7
	s_or_b64 s[2:3], s[2:3], vcc
	v_cndmask_b32_e64 v8, 0, 1, s[2:3]
	v_cmp_ne_u32_e32 vcc, 0, v8
	s_cmp_eq_u64 vcc, 0
	s_cselect_b64 s[2:3], -1, 0
	v_cndmask_b32_e64 v8, 0, 1, s[2:3]
	s_nop 0
	v_readfirstlane_b32 s2, v8
	s_bitcmp0_b32 s2, 0
	s_cbranch_scc0 .LBB4_45
	s_cmp_lt_i32 s28, 4
	s_cbranch_scc1 .LBB4_46
	s_cmp_gt_i32 s28, 4
	s_cbranch_scc0 .LBB4_47
	s_mov_b64 s[4:5], -1
	v_mov_b32_e32 v8, 0
	s_cmp_gt_i32 s28, 5
	v_mov_b32_e32 v167, 0
	v_mov_b32_e32 v166, 0
	v_mov_b32_e32 v165, 0
	v_mov_b32_e32 v164, 0
	v_mov_b32_e32 v162, 0
	v_mov_b32_e32 v160, 0
	v_mov_b32_e32 v159, 0
	v_mov_b32_e32 v157, 0
	v_mov_b32_e32 v151, 0
	v_mov_b32_e32 v149, 0
	v_mov_b32_e32 v147, 0
	v_mov_b32_e32 v146, 0
	v_mov_b32_e32 v144, 0
	v_mov_b32_e32 v143, 0
	v_mov_b32_e32 v152, 0
	v_mov_b32_e32 v153, 0
	v_mov_b32_e32 v154, 0
	v_mov_b32_e32 v155, 0
	v_mov_b32_e32 v156, 0
	v_mov_b32_e32 v158, 0
	v_mov_b32_e32 v161, 0
	v_mov_b32_e32 v163, 0
	v_mov_b32_e32 v168, 0
	v_mov_b32_e32 v169, 0
	v_mov_b32_e32 v170, 0
	v_mov_b32_e32 v171, 0
	v_mov_b32_e32 v172, 0
	v_mov_b32_e32 v173, 0
	v_mov_b32_e32 v174, 0
	v_mov_b32_e32 v145, 0
	v_mov_b32_e32 v148, 0
	v_mov_b32_e32 v150, 0
	s_cbranch_scc0 .LBB4_50
	s_cmp_eq_u32 s28, 6
	s_cbranch_scc0 .LBB4_49
	v_mov_b32_e32 v145, 0
	v_mov_b32_e32 v148, 0
	v_mov_b32_e32 v150, 0
	v_mov_b32_e32 v143, 0
	v_mov_b32_e32 v144, 0
	v_mov_b32_e32 v146, 0
	v_mov_b32_e32 v147, 0
	v_mov_b32_e32 v149, 0
	v_mov_b32_e32 v151, 0
	v_mov_b32_e32 v152, 0
	v_mov_b32_e32 v153, 0
	v_mov_b32_e32 v154, 0
	v_mov_b32_e32 v155, 0
	v_mov_b32_e32 v156, 0
	v_mov_b32_e32 v158, 0
	v_mov_b32_e32 v161, 0
	v_mov_b32_e32 v163, 0
	v_mov_b32_e32 v157, 0
	v_mov_b32_e32 v159, 0
	v_mov_b32_e32 v160, 0
	v_mov_b32_e32 v162, 0
	v_mov_b32_e32 v164, 0
	v_mov_b32_e32 v165, 0
	v_mov_b32_e32 v166, 0
	v_mov_b32_e32 v167, 0
	v_mov_b32_e32 v168, 0
	v_mov_b32_e32 v169, 0
	v_mov_b32_e32 v170, 0
	v_mov_b32_e32 v171, 0
	v_mov_b32_e32 v172, 0
	v_mov_b32_e32 v173, 0
	v_mov_b32_e32 v174, 0
	v_fma_mix_f32 v148, v43, v7, v148 op_sel_hi:[1,0,0]
	v_fma_mix_f32 v150, v45, v7, v150 op_sel_hi:[1,0,0]
	v_fma_mix_f32 v143, v50, v7, v143 op_sel_hi:[1,0,0]
	v_fma_mix_f32 v144, v54, v7, v144 op_sel_hi:[1,0,0]
	v_fma_mix_f32 v146, v58, v7, v146 op_sel_hi:[1,0,0]
	v_fma_mix_f32 v147, v61, v7, v147 op_sel_hi:[1,0,0]
	v_fma_mix_f32 v149, v64, v7, v149 op_sel_hi:[1,0,0]
	v_fma_mix_f32 v151, v66, v7, v151 op_sel_hi:[1,0,0]
	v_fma_mix_f32 v152, v43, v7, v152 op_sel:[1,0,0] op_sel_hi:[1,0,0]
	v_fma_mix_f32 v153, v45, v7, v153 op_sel:[1,0,0] op_sel_hi:[1,0,0]
	v_fma_mix_f32 v154, v50, v7, v154 op_sel:[1,0,0] op_sel_hi:[1,0,0]
	v_fma_mix_f32 v155, v54, v7, v155 op_sel:[1,0,0] op_sel_hi:[1,0,0]
	v_fma_mix_f32 v156, v58, v7, v156 op_sel:[1,0,0] op_sel_hi:[1,0,0]
	v_fma_mix_f32 v158, v61, v7, v158 op_sel:[1,0,0] op_sel_hi:[1,0,0]
	v_fma_mix_f32 v161, v64, v7, v161 op_sel:[1,0,0] op_sel_hi:[1,0,0]
	v_fma_mix_f32 v163, v66, v7, v163 op_sel:[1,0,0] op_sel_hi:[1,0,0]
	v_fma_mix_f32 v157, v72, v7, v157 op_sel_hi:[1,0,0]
	v_fma_mix_f32 v159, v76, v7, v159 op_sel_hi:[1,0,0]
	v_fma_mix_f32 v160, v83, v7, v160 op_sel_hi:[1,0,0]
	v_fma_mix_f32 v162, v85, v7, v162 op_sel_hi:[1,0,0]
	v_fma_mix_f32 v164, v89, v7, v164 op_sel_hi:[1,0,0]
	v_fma_mix_f32 v165, v92, v7, v165 op_sel_hi:[1,0,0]
	v_fma_mix_f32 v166, v95, v7, v166 op_sel_hi:[1,0,0]
	v_fma_mix_f32 v167, v96, v7, v167 op_sel_hi:[1,0,0]
	v_fma_mix_f32 v168, v72, v7, v168 op_sel:[1,0,0] op_sel_hi:[1,0,0]
	v_fma_mix_f32 v169, v76, v7, v169 op_sel:[1,0,0] op_sel_hi:[1,0,0]
	v_fma_mix_f32 v170, v83, v7, v170 op_sel:[1,0,0] op_sel_hi:[1,0,0]
	v_fma_mix_f32 v171, v85, v7, v171 op_sel:[1,0,0] op_sel_hi:[1,0,0]
	v_fma_mix_f32 v172, v89, v7, v172 op_sel:[1,0,0] op_sel_hi:[1,0,0]
	v_fma_mix_f32 v173, v92, v7, v173 op_sel:[1,0,0] op_sel_hi:[1,0,0]
	v_fma_mix_f32 v174, v95, v7, v174 op_sel:[1,0,0] op_sel_hi:[1,0,0]
	v_fma_mix_f32 v145, v96, v7, v145 op_sel:[1,0,0] op_sel_hi:[1,0,0]
	s_branch .LBB4_50

amdhsa.kernels:
  - .agpr_count:     0
    .args:
      - .actual_access:  read_only
        .address_space:  global
        .offset:         0
        .size:           8
        .value_kind:     global_buffer
      - .actual_access:  read_only
        .address_space:  global
        .offset:         8
        .size:           8
        .value_kind:     global_buffer
      - .actual_access:  read_only
        .address_space:  global
        .offset:         16
        .size:           8
        .value_kind:     global_buffer
      - .actual_access:  read_only
        .address_space:  global
        .offset:         24
        .size:           8
        .value_kind:     global_buffer
      - .actual_access:  write_only
        .address_space:  global
        .offset:         32
        .size:           8
        .value_kind:     global_buffer
      - .actual_access:  write_only
        .address_space:  global
        .offset:         40
        .size:           8
        .value_kind:     global_buffer
      - .actual_access:  write_only
        .address_space:  global
        .offset:         48
        .size:           8
        .value_kind:     global_buffer
      - .actual_access:  write_only
        .address_space:  global
        .offset:         56
        .size:           8
        .value_kind:     global_buffer
      - .actual_access:  write_only
        .address_space:  global
        .offset:         64
        .size:           8
        .value_kind:     global_buffer
      - .actual_access:  write_only
        .address_space:  global
        .offset:         72
        .size:           8
        .value_kind:     global_buffer
      - .actual_access:  write_only
        .address_space:  global
        .offset:         80
        .size:           8
        .value_kind:     global_buffer
      - .actual_access:  write_only
        .address_space:  global
        .offset:         88
        .size:           8
        .value_kind:     global_buffer
      - .actual_access:  write_only
        .address_space:  global
        .offset:         96
        .size:           8
        .value_kind:     global_buffer
      - .actual_access:  write_only
        .address_space:  global
        .offset:         104
        .size:           8
        .value_kind:     global_buffer
      - .actual_access:  write_only
        .address_space:  global
        .offset:         112
        .size:           8
        .value_kind:     global_buffer
    .group_segment_fixed_size: 67584
    .kernarg_segment_align: 8
    .kernarg_segment_size: 120
    .language:       OpenCL C
    .language_version:
      - 2
      - 0
    .max_flat_workgroup_size: 1024
    .name:           _Z6k_sortPKfS0_PKiS2_PiP15HIP_vector_typeIfLj4EEPfS7_S3_S7_S7_S3_S3_S6_S6_
    .private_segment_fixed_size: 0
    .sgpr_count:     58
    .sgpr_spill_count: 0
    .symbol:         _Z6k_sortPKfS0_PKiS2_PiP15HIP_vector_typeIfLj4EEPfS7_S3_S7_S7_S3_S3_S6_S6_.kd
    .uniform_work_group_size: 1
    .uses_dynamic_stack: false
    .vgpr_count:     48
    .vgpr_spill_count: 0
    .wavefront_size: 64
  - .agpr_count:     0
    .args:
      - .actual_access:  read_only
        .address_space:  global
        .offset:         0
        .size:           8
        .value_kind:     global_buffer
      - .actual_access:  read_only
        .address_space:  global
        .offset:         8
        .size:           8
        .value_kind:     global_buffer
      - .actual_access:  read_only
        .address_space:  global
        .offset:         16
        .size:           8
        .value_kind:     global_buffer
      - .actual_access:  read_only
        .address_space:  global
        .offset:         24
        .size:           8
        .value_kind:     global_buffer
      - .actual_access:  read_only
        .address_space:  global
        .offset:         32
        .size:           8
        .value_kind:     global_buffer
      - .actual_access:  read_only
        .address_space:  global
        .offset:         40
        .size:           8
        .value_kind:     global_buffer
      - .actual_access:  read_only
        .address_space:  global
        .offset:         48
        .size:           8
        .value_kind:     global_buffer
      - .actual_access:  write_only
        .address_space:  global
        .offset:         56
        .size:           8
        .value_kind:     global_buffer
    .group_segment_fixed_size: 145952
    .kernarg_segment_align: 8
    .kernarg_segment_size: 64
    .language:       OpenCL C
    .language_version:
      - 2
      - 0
    .max_flat_workgroup_size: 512
    .name:           _Z7k_finalPK15HIP_vector_typeIfLj4EES2_PKiS4_PKfS6_PKDF16_Pf
    .private_segment_fixed_size: 0
    .sgpr_count:     34
    .sgpr_spill_count: 0
    .symbol:         _Z7k_finalPK15HIP_vector_typeIfLj4EES2_PKiS4_PKfS6_PKDF16_Pf.kd
    .uniform_work_group_size: 1
    .uses_dynamic_stack: false
    .vgpr_count:     177
    .vgpr_spill_count: 0
    .wavefront_size: 64
  - .agpr_count:     0
    .args:
      - .actual_access:  read_only
        .address_space:  global
        .offset:         0
        .size:           8
        .value_kind:     global_buffer
      - .actual_access:  read_only
        .address_space:  global
        .offset:         8
        .size:           8
        .value_kind:     global_buffer
      - .actual_access:  read_only
        .address_space:  global
        .offset:         16
        .size:           8
        .value_kind:     global_buffer
      - .actual_access:  read_only
        .address_space:  global
        .offset:         24
        .size:           8
        .value_kind:     global_buffer
      - .actual_access:  read_only
        .address_space:  global
        .offset:         32
        .size:           8
        .value_kind:     global_buffer
      - .actual_access:  read_only
        .address_space:  global
        .offset:         40
        .size:           8
        .value_kind:     global_buffer
      - .actual_access:  read_only
        .address_space:  global
        .offset:         48
        .size:           8
        .value_kind:     global_buffer
      - .actual_access:  read_only
        .address_space:  global
        .offset:         56
        .size:           8
        .value_kind:     global_buffer
      - .actual_access:  read_only
        .address_space:  global
        .offset:         64
        .size:           8
        .value_kind:     global_buffer
      - .address_space:  global
        .offset:         72
        .size:           8
        .value_kind:     global_buffer
      - .actual_access:  read_only
        .address_space:  global
        .offset:         80
        .size:           8
        .value_kind:     global_buffer
      - .actual_access:  read_only
        .address_space:  global
        .offset:         88
        .size:           8
        .value_kind:     global_buffer
      - .actual_access:  read_only
        .address_space:  global
        .offset:         96
        .size:           8
        .value_kind:     global_buffer
      - .actual_access:  write_only
        .address_space:  global
        .offset:         104
        .size:           8
        .value_kind:     global_buffer
      - .address_space:  global
        .offset:         112
        .size:           8
        .value_kind:     global_buffer
      - .actual_access:  write_only
        .address_space:  global
        .offset:         120
        .size:           8
        .value_kind:     global_buffer
      - .actual_access:  write_only
        .address_space:  global
        .offset:         128
        .size:           8
        .value_kind:     global_buffer
      - .actual_access:  write_only
        .address_space:  global
        .offset:         136
        .size:           8
        .value_kind:     global_buffer
      - .actual_access:  write_only
        .address_space:  global
        .offset:         144
        .size:           8
        .value_kind:     global_buffer
    .group_segment_fixed_size: 30384
    .kernarg_segment_align: 8
    .kernarg_segment_size: 152
    .language:       OpenCL C
    .language_version:
      - 2
      - 0
    .max_flat_workgroup_size: 512
    .name:           _Z6k_iterILb1ELb0EEvPKfS1_PKiPK15HIP_vector_typeIfLj4EES7_S1_S1_S3_S1_PfS8_S1_S3_PDF16_PS5_SA_PiSA_SB_
    .private_segment_fixed_size: 0
    .sgpr_count:     102
    .sgpr_spill_count: 0
    .symbol:         _Z6k_iterILb1ELb0EEvPKfS1_PKiPK15HIP_vector_typeIfLj4EES7_S1_S1_S3_S1_PfS8_S1_S3_PDF16_PS5_SA_PiSA_SB_.kd
    .uniform_work_group_size: 1
    .uses_dynamic_stack: false
    .vgpr_count:     256
    .vgpr_spill_count: 0
    .wavefront_size: 64
  - .agpr_count:     0
    .args:
      - .actual_access:  read_only
        .address_space:  global
        .offset:         0
        .size:           8
        .value_kind:     global_buffer
      - .actual_access:  read_only
        .address_space:  global
        .offset:         8
        .size:           8
        .value_kind:     global_buffer
      - .actual_access:  read_only
        .address_space:  global
        .offset:         16
        .size:           8
        .value_kind:     global_buffer
      - .actual_access:  read_only
        .address_space:  global
        .offset:         24
        .size:           8
        .value_kind:     global_buffer
      - .actual_access:  read_only
        .address_space:  global
        .offset:         32
        .size:           8
        .value_kind:     global_buffer
      - .actual_access:  read_only
        .address_space:  global
        .offset:         40
        .size:           8
        .value_kind:     global_buffer
      - .actual_access:  read_only
        .address_space:  global
        .offset:         48
        .size:           8
        .value_kind:     global_buffer
      - .actual_access:  read_only
        .address_space:  global
        .offset:         56
        .size:           8
        .value_kind:     global_buffer
      - .actual_access:  read_only
        .address_space:  global
        .offset:         64
        .size:           8
        .value_kind:     global_buffer
      - .address_space:  global
        .offset:         72
        .size:           8
        .value_kind:     global_buffer
      - .actual_access:  read_only
        .address_space:  global
        .offset:         80
        .size:           8
        .value_kind:     global_buffer
      - .actual_access:  read_only
        .address_space:  global
        .offset:         88
        .size:           8
        .value_kind:     global_buffer
      - .actual_access:  read_only
        .address_space:  global
        .offset:         96
        .size:           8
        .value_kind:     global_buffer
      - .actual_access:  read_only
        .address_space:  global
        .offset:         104
        .size:           8
        .value_kind:     global_buffer
      - .actual_access:  read_only
        .address_space:  global
        .offset:         112
        .size:           8
        .value_kind:     global_buffer
      - .actual_access:  read_only
        .address_space:  global
        .offset:         120
        .size:           8
        .value_kind:     global_buffer
      - .actual_access:  read_only
        .address_space:  global
        .offset:         128
        .size:           8
        .value_kind:     global_buffer
      - .actual_access:  read_only
        .address_space:  global
        .offset:         136
        .size:           8
        .value_kind:     global_buffer
      - .actual_access:  read_only
        .address_space:  global
        .offset:         144
        .size:           8
        .value_kind:     global_buffer
    .group_segment_fixed_size: 5808
    .kernarg_segment_align: 8
    .kernarg_segment_size: 152
    .language:       OpenCL C
    .language_version:
      - 2
      - 0
    .max_flat_workgroup_size: 512
    .name:           _Z6k_iterILb0ELb0EEvPKfS1_PKiPK15HIP_vector_typeIfLj4EES7_S1_S1_S3_S1_PfS8_S1_S3_PDF16_PS5_SA_PiSA_SB_
    .private_segment_fixed_size: 0
    .sgpr_count:     46
    .sgpr_spill_count: 0
    .symbol:         _Z6k_iterILb0ELb0EEvPKfS1_PKiPK15HIP_vector_typeIfLj4EES7_S1_S1_S3_S1_PfS8_S1_S3_PDF16_PS5_SA_PiSA_SB_.kd
    .uniform_work_group_size: 1
    .uses_dynamic_stack: false
    .vgpr_count:     184
    .vgpr_spill_count: 0
    .wavefront_size: 64
  - .agpr_count:     0
    .args:
      - .actual_access:  read_only
        .address_space:  global
        .offset:         0
        .size:           8
        .value_kind:     global_buffer
      - .actual_access:  read_only
        .address_space:  global
        .offset:         8
        .size:           8
        .value_kind:     global_buffer
      - .actual_access:  read_only
        .address_space:  global
        .offset:         16
        .size:           8
        .value_kind:     global_buffer
      - .actual_access:  read_only
        .address_space:  global
        .offset:         24
        .size:           8
        .value_kind:     global_buffer
      - .actual_access:  read_only
        .address_space:  global
        .offset:         32
        .size:           8
        .value_kind:     global_buffer
      - .actual_access:  read_only
        .address_space:  global
        .offset:         40
        .size:           8
        .value_kind:     global_buffer
      - .actual_access:  read_only
        .address_space:  global
        .offset:         48
        .size:           8
        .value_kind:     global_buffer
      - .actual_access:  read_only
        .address_space:  global
        .offset:         56
        .size:           8
        .value_kind:     global_buffer
      - .actual_access:  read_only
        .address_space:  global
        .offset:         64
        .size:           8
        .value_kind:     global_buffer
      - .address_space:  global
        .offset:         72
        .size:           8
        .value_kind:     global_buffer
      - .actual_access:  write_only
        .address_space:  global
        .offset:         80
        .size:           8
        .value_kind:     global_buffer
      - .actual_access:  read_only
        .address_space:  global
        .offset:         88
        .size:           8
        .value_kind:     global_buffer
      - .actual_access:  read_only
        .address_space:  global
        .offset:         96
        .size:           8
        .value_kind:     global_buffer
      - .actual_access:  read_only
        .address_space:  global
        .offset:         104
        .size:           8
        .value_kind:     global_buffer
      - .actual_access:  read_only
        .address_space:  global
        .offset:         112
        .size:           8
        .value_kind:     global_buffer
      - .actual_access:  read_only
        .address_space:  global
        .offset:         120
        .size:           8
        .value_kind:     global_buffer
      - .actual_access:  read_only
        .address_space:  global
        .offset:         128
        .size:           8
        .value_kind:     global_buffer
      - .actual_access:  read_only
        .address_space:  global
        .offset:         136
        .size:           8
        .value_kind:     global_buffer
      - .actual_access:  read_only
        .address_space:  global
        .offset:         144
        .size:           8
        .value_kind:     global_buffer
    .group_segment_fixed_size: 5808
    .kernarg_segment_align: 8
    .kernarg_segment_size: 152
    .language:       OpenCL C
    .language_version:
      - 2
      - 0
    .max_flat_workgroup_size: 512
    .name:           _Z6k_iterILb0ELb1EEvPKfS1_PKiPK15HIP_vector_typeIfLj4EES7_S1_S1_S3_S1_PfS8_S1_S3_PDF16_PS5_SA_PiSA_SB_
    .private_segment_fixed_size: 0
    .sgpr_count:     46
    .sgpr_spill_count: 0
    .symbol:         _Z6k_iterILb0ELb1EEvPKfS1_PKiPK15HIP_vector_typeIfLj4EES7_S1_S1_S3_S1_PfS8_S1_S3_PDF16_PS5_SA_PiSA_SB_.kd
    .uniform_work_group_size: 1
    .uses_dynamic_stack: false
    .vgpr_count:     184
    .vgpr_spill_count: 0
    .wavefront_size: 64
